# s15 + small_from_hn: A-fragment rows prefetched before the w_small staging loads and consumed from registers (two load->wait->MFMA batches removed)
# speedup vs baseline: 1.0005x; 1.0005x over previous
; #define PG8_LAS __attribute__((address_space(3)))
; __device__ __forceinline__ void small_from_hn(const h16* __restrict__ hn, const h16* __restrict__ wsm16  , const float* __restrict__ fox_bf, const float* __restrict__ ml_bi, ...
;     int tid_ = threadIdx.x; asm volatile("" : "+v"(tid_));
;     const int lane = tid_ & 63, wave = tid_ >> 6;
;     constexpr int WP = 1032;
; #pragma unroll
;     for (int q = 0; q < 4; ++q) { const int e = (q * NTHREADS + tid_) * 8, c = e >> 10, k = e & 1023;
;         *(PG8_LAS h16x8*)(L + (c * WP + k) * 2) = *(const h16x8*)(wsm16 + e); }
;     asm volatile("s_waitcnt vmcnt(0) lgkmcnt(0)" ::: "memory"); __syncthreads();
;     if (wave < 4) {
;         for (int blk = blockIdx.x; blk < TH / 64; blk += gridDim.x) {
;             const int R0 = blk * 64 + 16 * wave, i = lane & 15, gq = lane >> 4;
;             const h16* xr = hn + (size_t)(R0 + i) * DM + 8 * gq;
;             const PG8_LAS unsigned char* wr = L + (i * WP + 8 * gq) * 2;
;             f32x4 acc = {0.f, 0.f, 0.f, 0.f};
; #pragma unroll 1
;             for (int kb = 0; kb < 32; kb += 16) {
;                 h16x8 av[16];
; #pragma unroll
;                 for (int u = 0; u < 16; ++u) av[u] = *(const h16x8*)(xr + 32 * (kb + u));
.LBB0_932:
	v_readlane_b32 s0, v255, 32
	s_cmp_eq_u32 s0, 1
	s_cbranch_scc0 .LBB0_1000
	v_readlane_b32 s0, v255, 31
	s_cmp_lt_u32 s0, 2
	v_readlane_b32 s0, v253, 54
	v_readlane_b32 s2, v253, 56
	v_readlane_b32 s1, v253, 55
	s_cselect_b32 s0, s0, s2
	v_readlane_b32 s2, v253, 57
	s_cselect_b32 s1, s1, s2
	v_readlane_b32 s2, v255, 42
	s_cmp_eq_u32 s2, 0
	v_readlane_b32 s2, v253, 24
	v_readlane_b32 s3, v253, 25
	s_cselect_b32 s3, s3, s1
	s_cselect_b32 s2, s2, s0
	v_readlane_b32 s0, v255, 36
	s_lshl_b32 s0, s0, 15
	v_readlane_b32 s4, v254, 2
	v_mov_b32_e32 v0, v243
	v_readfirstlane_b32 s100, v243
	s_cmp_lt_u32 s100, 0x100
	s_mov_b32 s101, 0
	s_cbranch_scc0 .Lsm_pfdone
	v_readlane_b32 s100, v252, 0
	v_lshrrev_b32_e32 v122, 6, v243
	v_lshlrev_b32_e32 v122, 4, v122
	v_and_b32_e32 v123, 15, v243
	v_or_b32_e32 v122, v122, v123
	s_lshl_b32 s100, s100, 6
	v_add_u32_e32 v122, s100, v122
	v_mov_b32_e32 v123, 0
	v_lshlrev_b64 v[122:123], 11, v[122:123]
	v_bfe_u32 v124, v243, 4, 2
	v_lshlrev_b32_e32 v124, 4, v124
	v_mov_b32_e32 v125, 0
	v_lshl_add_u64 v[122:123], s[2:3], 0, v[122:123]
	v_lshl_add_u64 v[122:123], v[122:123], 0, v[124:125]
	global_load_dwordx4 v[100:103], v[122:123], off
	global_load_dwordx4 v[104:107], v[122:123], off offset:64
	global_load_dwordx4 v[108:111], v[122:123], off offset:128
	global_load_dwordx4 v[112:115], v[122:123], off offset:192
	global_load_dwordx4 v[116:119], v[122:123], off offset:256
	global_load_dwordx4 v[128:131], v[122:123], off offset:320
	global_load_dwordx4 v[132:135], v[122:123], off offset:384
	global_load_dwordx4 v[136:139], v[122:123], off offset:448
	global_load_dwordx4 v[140:143], v[122:123], off offset:512
	global_load_dwordx4 v[144:147], v[122:123], off offset:576
	global_load_dwordx4 v[148:151], v[122:123], off offset:640
	global_load_dwordx4 v[152:155], v[122:123], off offset:704
	global_load_dwordx4 v[156:159], v[122:123], off offset:768
	global_load_dwordx4 v[160:163], v[122:123], off offset:832
	global_load_dwordx4 v[164:167], v[122:123], off offset:896
	global_load_dwordx4 v[168:171], v[122:123], off offset:960
	global_load_dwordx4 v[172:175], v[122:123], off offset:1024
	global_load_dwordx4 v[176:179], v[122:123], off offset:1088
	global_load_dwordx4 v[180:183], v[122:123], off offset:1152
	global_load_dwordx4 v[184:187], v[122:123], off offset:1216
	global_load_dwordx4 v[188:191], v[122:123], off offset:1280
	global_load_dwordx4 v[192:195], v[122:123], off offset:1344
	global_load_dwordx4 v[196:199], v[122:123], off offset:1408
	global_load_dwordx4 v[200:203], v[122:123], off offset:1472
	global_load_dwordx4 v[204:207], v[122:123], off offset:1536
	global_load_dwordx4 v[208:211], v[122:123], off offset:1600
	global_load_dwordx4 v[212:215], v[122:123], off offset:1664
	global_load_dwordx4 v[216:219], v[122:123], off offset:1728
	global_load_dwordx4 v[220:223], v[122:123], off offset:1792
	global_load_dwordx4 v[224:227], v[122:123], off offset:1856
	global_load_dwordx4 v[228:231], v[122:123], off offset:1920
	global_load_dwordx4 v[232:235], v[122:123], off offset:1984
	s_mov_b32 s101, 1
.Lsm_pfdone:
	v_readlane_b32 s1, v255, 37
	v_readlane_b32 s5, v254, 3
	s_add_u32 s0, s4, s0
	s_addc_u32 s1, s5, 0
	v_lshlrev_b32_e32 v6, 3, v0
	v_ashrrev_i32_e32 v7, 31, v6
	v_lshl_add_u64 v[2:3], v[6:7], 1, s[0:1]
	global_load_dwordx4 v[2:5], v[2:3], off
	v_and_b32_e32 v1, 0x3f8, v6
	v_bfe_i32 v8, v0, 7, 22
	s_movk_i32 s4, 0x408
	v_mad_i32_i24 v7, v8, s4, v1
	v_lshl_add_u32 v7, v7, 1, 0
	v_add_u32_e32 v12, 0x1000, v6
	v_ashrrev_i32_e32 v13, 31, v12
	v_ashrrev_i32_e32 v9, 10, v12
	v_lshl_add_u64 v[12:13], v[12:13], 1, s[0:1]
	global_load_dwordx4 v[12:15], v[12:13], off
	v_mad_i32_i24 v9, v9, s4, v1
	v_lshl_add_u32 v9, v9, 1, 0
	v_add_u32_e32 v16, 0x2000, v6
	v_ashrrev_i32_e32 v17, 31, v16
	v_ashrrev_i32_e32 v10, 10, v16
	v_lshl_add_u64 v[16:17], v[16:17], 1, s[0:1]
	global_load_dwordx4 v[16:19], v[16:17], off
	v_mad_i32_i24 v10, v10, s4, v1
	v_lshl_add_u32 v10, v10, 1, 0
	v_add_u32_e32 v20, 0x3000, v6
	v_ashrrev_i32_e32 v21, 31, v20
	v_ashrrev_i32_e32 v6, 10, v20
	v_lshl_add_u64 v[20:21], v[20:21], 1, s[0:1]
	global_load_dwordx4 v[20:23], v[20:21], off
	v_mad_i32_i24 v1, v6, s4, v1
	v_lshl_add_u32 v1, v1, 1, 0
	v_readlane_b32 s0, v254, 63
	v_readlane_b32 s1, v255, 0
	s_waitcnt vmcnt(3)
	ds_write_b128 v7, v[2:5]
	s_waitcnt vmcnt(2)
	ds_write_b128 v9, v[12:15]
	s_waitcnt vmcnt(1)
	ds_write_b128 v10, v[16:19]
	s_waitcnt vmcnt(0)
	ds_write_b128 v1, v[20:23]
	v_ashrrev_i32_e32 v1, 6, v0
	s_waitcnt vmcnt(0) lgkmcnt(0)
	v_cmp_gt_i32_e32 vcc, 4, v1
	s_and_b64 s[0:1], vcc, s[0:1]
	s_waitcnt lgkmcnt(0)
	s_barrier
	s_and_saveexec_b64 s[14:15], s[0:1]
	s_cbranch_execz .LBB0_971
	v_readlane_b32 s0, v255, 36
	v_readlane_b32 s1, v255, 37
	s_lshl_b32 s28, s0, 2
	v_readlane_b32 s52, v253, 36
	s_mov_b32 s6, s0
	s_lshl_b64 s[0:1], s[28:29], 2
	v_readlane_b32 s64, v253, 48
	v_readlane_b32 s65, v253, 49
	s_add_u32 s4, s64, s0
	v_readlane_b32 s62, v253, 46
	s_addc_u32 s5, s65, s1
	v_lshlrev_b32_e32 v76, 4, v1
	v_and_b32_e32 v77, 15, v0
	v_bfe_u32 v1, v0, 4, 2
	v_readlane_b32 s63, v253, 47
	s_add_u32 s0, s62, s0
	v_lshlrev_b32_e32 v96, 4, v1
	v_mul_u32_u24_e32 v2, 0x408, v77
	s_addc_u32 s1, s63, s1
	s_lshl_b32 s28, s6, 3
	v_lshl_add_u64 v[68:69], s[2:3], 0, v[96:97]
	v_lshl_add_u32 v2, v1, 3, v2
	v_lshlrev_b32_e32 v96, 2, v77
	v_readlane_b32 s58, v253, 42
	s_lshl_b64 s[10:11], s[28:29], 2
	v_lshl_add_u32 v78, v2, 1, 0
	v_lshl_add_u64 v[2:3], s[4:5], 0, v[96:97]
	s_movk_i32 s4, 0xffd0
	v_lshl_add_u64 v[4:5], s[0:1], 0, v[96:97]
	s_movk_i32 s0, 0xffe0
	v_readlane_b32 s59, v253, 43
	s_add_u32 s10, s58, s10
	s_mov_b32 s5, -1
	s_mov_b32 s1, -1
	s_addc_u32 s11, s59, s11
	v_lshl_add_u64 v[2:3], v[2:3], 0, s[4:5]
	v_lshl_add_u64 v[4:5], v[4:5], 0, s[0:1]
	v_and_b32_e32 v0, 12, v0
	v_readlane_b32 s0, v255, 43
	v_cmp_gt_u32_e32 vcc, 12, v77
	v_lshl_add_u64 v[6:7], s[10:11], 0, v[96:97]
	v_cmp_ne_u32_e64 s[38:39], 8, v0
	v_lshl_or_b32 v79, v1, 2, s0
	v_cndmask_b32_e32 v0, v2, v4, vcc
	v_cndmask_b32_e32 v1, v3, v5, vcc
	v_cmp_gt_u32_e32 vcc, 8, v77
	v_lshl_add_u64 v[70:71], s[86:87], 0, v[96:97]
	v_readlane_b32 s4, v252, 0
	v_cndmask_b32_e32 v73, v1, v7, vcc
	v_cndmask_b32_e32 v72, v0, v6, vcc
	global_load_dword v120, v[72:73], off
	v_readlane_b32 s53, v253, 37
	v_readlane_b32 s54, v253, 38
	v_readlane_b32 s55, v253, 39
	v_readlane_b32 s56, v253, 40
	v_readlane_b32 s57, v253, 41
	v_readlane_b32 s60, v253, 44
	v_readlane_b32 s61, v253, 45
	v_readlane_b32 s66, v253, 50
	v_readlane_b32 s67, v253, 51
	s_branch .LBB0_946

; #define PG8_LAS __attribute__((address_space(3)))
; __device__ __forceinline__ void small_from_hn(const h16* __restrict__ hn, const h16* __restrict__ wsm16  , const float* __restrict__ fox_bf, const float* __restrict__ ml_bi, ...
;     ...
;         for (int blk = blockIdx.x; blk < TH / 64; blk += gridDim.x) {
;             const int R0 = blk * 64 + 16 * wave, i = lane & 15, gq = lane >> 4;
;             const h16* xr = hn + (size_t)(R0 + i) * DM + 8 * gq;
;             const PG8_LAS unsigned char* wr = L + (i * WP + 8 * gq) * 2;
;             f32x4 acc = {0.f, 0.f, 0.f, 0.f};
; #pragma unroll 1
;             for (int kb = 0; kb < 32; kb += 16) {
;                 h16x8 av[16];
; #pragma unroll
;                 for (int u = 0; u < 16; ++u) av[u] = *(const h16x8*)(xr + 32 * (kb + u));
;                 asm volatile("" ::: "memory");
; #pragma unroll
;                 for (int u = 0; u < 16; ++u) { const h16x8 bv = *(const PG8_LAS h16x8*)(wr + 64 * (kb + u));
;                     acc = __builtin_amdgcn_mfma_f32_16x16x32_f16(av[u], bv, acc, 0, 0, 0); }
;             }
.LBB0_946:
	v_lshl_add_u32 v80, s4, 6, v76
	v_or_b32_e32 v0, v80, v77
	v_ashrrev_i32_e32 v1, 31, v0
	v_lshlrev_b64 v[0:1], 11, v[0:1]
	v_lshl_add_u64 v[74:75], v[68:69], 0, v[0:1]
	v_mov_b32_e32 v0, 0
	s_mov_b32 s5, 0
	s_mov_b64 s[0:1], -1
	v_mov_b32_e32 v1, v0
	v_mov_b32_e32 v2, v0
	v_mov_b32_e32 v3, v0
	s_cmp_eq_u32 s101, 1
	s_cbranch_scc0 .LBB0_947
	s_mov_b32 s101, 0
	s_waitcnt vmcnt(0)
	ds_read_b128 v[4:7], v78
	ds_read_b128 v[8:11], v78 offset:64
	s_waitcnt lgkmcnt(1)
	v_mfma_f32_16x16x32_f16 v[0:3], v[100:103], v[4:7], v[0:3]
	ds_read_b128 v[4:7], v78 offset:128
	s_waitcnt lgkmcnt(1)
	v_mfma_f32_16x16x32_f16 v[0:3], v[104:107], v[8:11], v[0:3]
	ds_read_b128 v[8:11], v78 offset:192
	s_waitcnt lgkmcnt(1)
	v_mfma_f32_16x16x32_f16 v[0:3], v[108:111], v[4:7], v[0:3]
	ds_read_b128 v[4:7], v78 offset:256
	s_waitcnt lgkmcnt(1)
	v_mfma_f32_16x16x32_f16 v[0:3], v[112:115], v[8:11], v[0:3]
	ds_read_b128 v[8:11], v78 offset:320
	s_waitcnt lgkmcnt(1)
	v_mfma_f32_16x16x32_f16 v[0:3], v[116:119], v[4:7], v[0:3]
	ds_read_b128 v[4:7], v78 offset:384
	s_waitcnt lgkmcnt(1)
	v_mfma_f32_16x16x32_f16 v[0:3], v[128:131], v[8:11], v[0:3]
	ds_read_b128 v[8:11], v78 offset:448
	s_waitcnt lgkmcnt(1)
	v_mfma_f32_16x16x32_f16 v[0:3], v[132:135], v[4:7], v[0:3]
	ds_read_b128 v[4:7], v78 offset:512
	s_waitcnt lgkmcnt(1)
	v_mfma_f32_16x16x32_f16 v[0:3], v[136:139], v[8:11], v[0:3]
	ds_read_b128 v[8:11], v78 offset:576
	s_waitcnt lgkmcnt(1)
	v_mfma_f32_16x16x32_f16 v[0:3], v[140:143], v[4:7], v[0:3]
	ds_read_b128 v[4:7], v78 offset:640
	s_waitcnt lgkmcnt(1)
	v_mfma_f32_16x16x32_f16 v[0:3], v[144:147], v[8:11], v[0:3]
	ds_read_b128 v[8:11], v78 offset:704
	s_waitcnt lgkmcnt(1)
	v_mfma_f32_16x16x32_f16 v[0:3], v[148:151], v[4:7], v[0:3]
	ds_read_b128 v[4:7], v78 offset:768
	s_waitcnt lgkmcnt(1)
	v_mfma_f32_16x16x32_f16 v[0:3], v[152:155], v[8:11], v[0:3]
	ds_read_b128 v[8:11], v78 offset:832
	s_waitcnt lgkmcnt(1)
	v_mfma_f32_16x16x32_f16 v[0:3], v[156:159], v[4:7], v[0:3]
	ds_read_b128 v[4:7], v78 offset:896
	s_waitcnt lgkmcnt(1)
	v_mfma_f32_16x16x32_f16 v[0:3], v[160:163], v[8:11], v[0:3]
	ds_read_b128 v[8:11], v78 offset:960
	s_waitcnt lgkmcnt(1)
	v_mfma_f32_16x16x32_f16 v[0:3], v[164:167], v[4:7], v[0:3]
	ds_read_b128 v[4:7], v78 offset:1024
	s_waitcnt lgkmcnt(1)
	v_mfma_f32_16x16x32_f16 v[0:3], v[168:171], v[8:11], v[0:3]
	ds_read_b128 v[8:11], v78 offset:1088
	s_waitcnt lgkmcnt(1)
	v_mfma_f32_16x16x32_f16 v[0:3], v[172:175], v[4:7], v[0:3]
	ds_read_b128 v[4:7], v78 offset:1152
	s_waitcnt lgkmcnt(1)
	v_mfma_f32_16x16x32_f16 v[0:3], v[176:179], v[8:11], v[0:3]
	ds_read_b128 v[8:11], v78 offset:1216
	s_waitcnt lgkmcnt(1)
	v_mfma_f32_16x16x32_f16 v[0:3], v[180:183], v[4:7], v[0:3]
	ds_read_b128 v[4:7], v78 offset:1280
	s_waitcnt lgkmcnt(1)
	v_mfma_f32_16x16x32_f16 v[0:3], v[184:187], v[8:11], v[0:3]
	ds_read_b128 v[8:11], v78 offset:1344
	s_waitcnt lgkmcnt(1)
	v_mfma_f32_16x16x32_f16 v[0:3], v[188:191], v[4:7], v[0:3]
	ds_read_b128 v[4:7], v78 offset:1408
	s_waitcnt lgkmcnt(1)
	v_mfma_f32_16x16x32_f16 v[0:3], v[192:195], v[8:11], v[0:3]
	ds_read_b128 v[8:11], v78 offset:1472
	s_waitcnt lgkmcnt(1)
	v_mfma_f32_16x16x32_f16 v[0:3], v[196:199], v[4:7], v[0:3]
	ds_read_b128 v[4:7], v78 offset:1536
	s_waitcnt lgkmcnt(1)
	v_mfma_f32_16x16x32_f16 v[0:3], v[200:203], v[8:11], v[0:3]
	ds_read_b128 v[8:11], v78 offset:1600
	s_waitcnt lgkmcnt(1)
	v_mfma_f32_16x16x32_f16 v[0:3], v[204:207], v[4:7], v[0:3]
	ds_read_b128 v[4:7], v78 offset:1664
	s_waitcnt lgkmcnt(1)
	v_mfma_f32_16x16x32_f16 v[0:3], v[208:211], v[8:11], v[0:3]
	ds_read_b128 v[8:11], v78 offset:1728
	s_waitcnt lgkmcnt(1)
	v_mfma_f32_16x16x32_f16 v[0:3], v[212:215], v[4:7], v[0:3]
	ds_read_b128 v[4:7], v78 offset:1792
	s_waitcnt lgkmcnt(1)
	v_mfma_f32_16x16x32_f16 v[0:3], v[216:219], v[8:11], v[0:3]
	ds_read_b128 v[8:11], v78 offset:1856
	s_waitcnt lgkmcnt(1)
	v_mfma_f32_16x16x32_f16 v[0:3], v[220:223], v[4:7], v[0:3]
	ds_read_b128 v[4:7], v78 offset:1920
	s_waitcnt lgkmcnt(1)
	v_mfma_f32_16x16x32_f16 v[0:3], v[224:227], v[8:11], v[0:3]
	ds_read_b128 v[8:11], v78 offset:1984
	s_waitcnt lgkmcnt(1)
	v_mfma_f32_16x16x32_f16 v[0:3], v[228:231], v[4:7], v[0:3]
	s_waitcnt lgkmcnt(0)
	v_mfma_f32_16x16x32_f16 v[0:3], v[232:235], v[8:11], v[0:3]
	s_mov_b32 s5, 16
	s_movk_i32 s28, 0x400
	s_mov_b64 s[0:1], 0
	s_mov_b64 vcc, exec
	s_branch .Lsm_after

; __device__ __forceinline__ void small_from_hn(const h16* __restrict__ hn, const h16* __restrict__ wsm16  , const float* __restrict__ fox_bf, const float* __restrict__ ml_bi, ...
;     ...
;             const float bias = i < 8 ? fox_bf[i] : i < 12 ? ml_bi[i - 8] : ml_bf[i - 12];
; #pragma unroll
;             for (int r = 0; r < 4; ++r) {
;                 const float pre = acc[r] + bias;
;                 small[(size_t)(row0 + R0 + 4 * gq + r) * 16 + i] = (i >= 8 && i < 12) ? pre : log_sigmoidf_(pre);
.Lsm_after:
	v_mov_b32_e32 v6, v120
	s_waitcnt vmcnt(0)
	s_nop 4
	v_add_f32_e32 v0, v0, v6
	s_and_saveexec_b64 s[20:21], s[38:39]
	s_cbranch_execz .LBB0_954
	s_mov_b32 s0, 0xbfb8aa3b
	v_mul_f32_e64 v4, |v0|, s0
	v_exp_f32_e32 v5, v4
	s_mov_b32 s0, 0x3c23d70a
	v_cmp_ngt_f32_e32 vcc, s0, v5
	s_and_saveexec_b64 s[0:1], vcc
	s_xor_b64 s[40:41], exec, s[0:1]
	s_cbranch_execz .LBB0_951
	v_add_f32_e32 v4, 1.0, v5
	v_cmp_gt_f32_e32 vcc, s44, v4
	s_mov_b32 s0, 0x3f317217
	s_nop 0
	v_cndmask_b32_e64 v5, 0, 32, vcc
	v_ldexp_f32 v4, v4, v5
	v_log_f32_e32 v4, v4
	s_nop 0
	v_mul_f32_e32 v5, 0x3f317217, v4
	v_fma_f32 v5, v4, s0, -v5
	v_fmac_f32_e32 v5, 0x3377d1cf, v4
	s_mov_b32 s0, 0x7f800000
	v_fmac_f32_e32 v5, 0x3f317217, v4
	v_cmp_lt_f32_e64 s[0:1], |v4|, s0
	s_nop 1
	v_cndmask_b32_e64 v4, v4, v5, s[0:1]
	v_cndmask_b32_e32 v5, 0, v244, vcc
	v_sub_f32_e32 v4, v4, v5
